# P3 conversion fill replaced by the hand-written block with two tiles of loads in flight per wave
# baseline (speedup 1.0000x reference)
; __device__ __forceinline__ void conv8_fill(const Ctx& X, int base, int rank, int nblk, int n) { conv8b_run(X, (base >> 3) + rank, nblk, n); }
; #define SEAM(k) do { if (IN(k) && IN((k) + 1)) xcd_barrier(bar); } while (0)
; __device__ __forceinline__ Cvb conv8b_dec(const Ctx& X, int bit) { Cvb c; int kb, nb;
;     if (bit < I_GU8 / 8) { const int e = bit >> 8, r = bit & 255; kb = r >> 4; nb = r & 15; c.N = 2 * DFF; c.W = XP_w_gu(X) + (size_t)e * D * (2 * DFF); c.WT = XP_WguT(X) + (size_t)e * 16 * PAN_GU + (size_t)kb * PAN_GU; }
;     else { const int b2 = bit - I_GU8 / 8, e = b2 >> 7, r = b2 & 127; kb = r >> 3; nb = r & 7; c.N = D; c.W = XP_w_d(X) + (size_t)e * DFF * D; c.WT = XP_WdT(X) + (size_t)e * 16 * PAN_D + (size_t)kb * PAN_D; }
;     c.W += (size_t)(kb * 128 + 16 * X.wave) * c.N + nb * 256 + 4 * X.lane;
;     c.WT += (size_t)(nb * 256 + 32 * X.wave + (X.lane >> 3)) * 128 + 16 * (X.lane & 7);
;     return c; }
; __device__ __forceinline__ void conv8b_run(const Ctx& X, int first, int step, int count) {
;     if (count <= 0) return;
;     f32x4 v[16];
;     Cvb c = conv8b_dec(X, first), cn = c;
; #pragma unroll
;     for (int i = 0; i < 16; ++i) v[i] = __builtin_nontemporal_load((const f32x4*)(c.W + (size_t)i * c.N));
; __global__ void __launch_bounds__(NTHR, 2) fwd(Args args) {
;     ...
;     if (IN(3)) { p3_scan(X); if (X.G == 256 && X.bid >= 192) conv8_fill(X, FILL_B3, X.bid - 192, FILL_W3 / NWAVES, FILL_N3); } SEAM(3);
.LBB0_474:
	s_or_b64 exec, exec, s[6:7]
	s_cmpk_lg_i32 s92, 0x100
	s_cselect_b64 s[2:3], -1, 0
	s_cmpk_lt_i32 s87, 0xc0
	s_cselect_b64 s[6:7], -1, 0
	s_or_b64 s[2:3], s[6:7], s[2:3]
	s_and_b64 vcc, exec, s[2:3]
	s_cbranch_vccnz .LBB0_480
	s_load_dwordx2 s[6:7], s[0:1], 0x70
	s_load_dwordx2 s[8:9], s[0:1], 0x80
	s_add_i32 s32, s87, 0x2900
	s_mov_b32 s33, 3
	s_mov_b32 s37, 0xc3e00000
	v_mov_b32_e32 v150, 0x43e00000
	v_lshlrev_b32_e32 v146, 4, v194
	v_mul_u32_u24_e32 v147, 0x240, v194
	s_lshl_b32 s34, s93, 4
	v_add_u32_e32 v147, s34, v147
	v_lshrrev_b32_e32 v151, 3, v194
	s_lshl_b32 s34, s93, 5
	v_add_u32_e32 v152, s34, v151
	v_mul_u32_u24_e32 v148, 0x90, v152
	v_and_b32_e32 v152, 7, v194
	v_lshl_add_u32 v148, v152, 4, v148
	v_lshlrev_b32_e32 v151, 7, v151
	v_lshl_add_u32 v149, v152, 4, v151
	s_waitcnt lgkmcnt(0)
	s_cmp_lt_u32 s32, 0x2000
	s_cbranch_scc0 .Lcv3_dnP0
	s_lshr_b32 s34, s32, 4
	s_lshl_b32 s34, s34, 21
	s_and_b32 s35, s32, 15
	s_lshl_b32 s35, s35, 10
	s_add_u32 s34, s34, s35
	s_lshl_b32 s35, s93, 18
	s_add_u32 s34, s34, s35
	s_add_u32 s10, s6, s34
	s_addc_u32 s11, s7, 0
	s_movk_i32 s12, 0x4000
	s_lshl_b32 s34, s32, 15
	s_add_u32 s34, s34, 0x30000000
	s_branch .Lcv3_cmP0
.Lcv3_dnP0:
	s_sub_u32 s36, s32, 0x2000
	s_lshr_b32 s34, s36, 3
	s_lshl_b32 s34, s34, 20
	s_and_b32 s35, s36, 7
	s_lshl_b32 s35, s35, 10
	s_add_u32 s34, s34, s35
	s_lshl_b32 s35, s93, 17
	s_add_u32 s34, s34, s35
	s_add_u32 s10, s8, s34
	s_addc_u32 s11, s9, 0
	s_movk_i32 s12, 0x2000
	s_lshl_b32 s34, s36, 15
	s_add_u32 s34, s34, 0x50000000
.Lcv3_cmP0:
	s_lshl_b32 s35, s93, 12
	s_add_u32 s34, s34, s35
	s_add_u32 s14, s90, s34
	s_addc_u32 s15, s91, 0
	global_load_dwordx4 v[2:5], v146, s[10:11] nt
	s_add_u32 s10, s10, s12
	s_addc_u32 s11, s11, 0
	global_load_dwordx4 v[6:9], v146, s[10:11] nt
	s_add_u32 s10, s10, s12
	s_addc_u32 s11, s11, 0
	global_load_dwordx4 v[10:13], v146, s[10:11] nt
	s_add_u32 s10, s10, s12
	s_addc_u32 s11, s11, 0
	global_load_dwordx4 v[14:17], v146, s[10:11] nt
	s_add_u32 s10, s10, s12
	s_addc_u32 s11, s11, 0
	global_load_dwordx4 v[18:21], v146, s[10:11] nt
	s_add_u32 s10, s10, s12
	s_addc_u32 s11, s11, 0
	global_load_dwordx4 v[22:25], v146, s[10:11] nt
	s_add_u32 s10, s10, s12
	s_addc_u32 s11, s11, 0
	global_load_dwordx4 v[26:29], v146, s[10:11] nt
	s_add_u32 s10, s10, s12
	s_addc_u32 s11, s11, 0
	global_load_dwordx4 v[30:33], v146, s[10:11] nt
	s_add_u32 s10, s10, s12
	s_addc_u32 s11, s11, 0
	global_load_dwordx4 v[34:37], v146, s[10:11] nt
	s_add_u32 s10, s10, s12
	s_addc_u32 s11, s11, 0
	global_load_dwordx4 v[38:41], v146, s[10:11] nt
	s_add_u32 s10, s10, s12
	s_addc_u32 s11, s11, 0
	global_load_dwordx4 v[42:45], v146, s[10:11] nt
	s_add_u32 s10, s10, s12
	s_addc_u32 s11, s11, 0
	global_load_dwordx4 v[46:49], v146, s[10:11] nt
	s_add_u32 s10, s10, s12
	s_addc_u32 s11, s11, 0
	global_load_dwordx4 v[50:53], v146, s[10:11] nt
	s_add_u32 s10, s10, s12
	s_addc_u32 s11, s11, 0
	global_load_dwordx4 v[54:57], v146, s[10:11] nt
	s_add_u32 s10, s10, s12
	s_addc_u32 s11, s11, 0
	global_load_dwordx4 v[58:61], v146, s[10:11] nt
	s_add_u32 s10, s10, s12
	s_addc_u32 s11, s11, 0
	global_load_dwordx4 v[62:65], v146, s[10:11] nt
	s_add_i32 s32, s32, 64
	s_add_i32 s33, s33, -1
	s_mov_b32 s38, 0
	s_cmp_eq_u32 s33, 0
	s_cbranch_scc1 .Lcv3_loop
	s_cmp_lt_u32 s32, 0x2000
	s_cbranch_scc0 .Lcv3_dnP1
	s_lshr_b32 s34, s32, 4
	s_lshl_b32 s34, s34, 21
	s_and_b32 s35, s32, 15
	s_lshl_b32 s35, s35, 10
	s_add_u32 s34, s34, s35
	s_lshl_b32 s35, s93, 18
	s_add_u32 s34, s34, s35
	s_add_u32 s10, s6, s34
	s_addc_u32 s11, s7, 0
	s_movk_i32 s12, 0x4000
	s_lshl_b32 s34, s32, 15
	s_add_u32 s34, s34, 0x30000000
	s_branch .Lcv3_cmP1

; __device__ __forceinline__ void conv8b_run(const Ctx& X, int first, int step, int count) {
;     ...
;     f32x4 v[16];
;     Cvb c = conv8b_dec(X, first), cn = c;
; #pragma unroll
;     for (int i = 0; i < 16; ++i) v[i] = __builtin_nontemporal_load((const f32x4*)(c.W + (size_t)i * c.N));
;     ...
;         if (j + 1 < count) { cn = conv8b_dec(X, first + (j + 1) * step);
; #pragma unroll
;             for (int i = 0; i < 16; ++i) v[i] = __builtin_nontemporal_load((const f32x4*)(cn.W + (size_t)i * cn.N)); }
.Lcv3_cmP1:
	s_lshl_b32 s35, s93, 12
	s_add_u32 s34, s34, s35
	s_add_u32 s16, s90, s34
	s_addc_u32 s17, s91, 0
	global_load_dwordx4 v[66:69], v146, s[10:11] nt
	s_add_u32 s10, s10, s12
	s_addc_u32 s11, s11, 0
	global_load_dwordx4 v[70:73], v146, s[10:11] nt
	s_add_u32 s10, s10, s12
	s_addc_u32 s11, s11, 0
	global_load_dwordx4 v[74:77], v146, s[10:11] nt
	s_add_u32 s10, s10, s12
	s_addc_u32 s11, s11, 0
	global_load_dwordx4 v[78:81], v146, s[10:11] nt
	s_add_u32 s10, s10, s12
	s_addc_u32 s11, s11, 0
	global_load_dwordx4 v[82:85], v146, s[10:11] nt
	s_add_u32 s10, s10, s12
	s_addc_u32 s11, s11, 0
	global_load_dwordx4 v[86:89], v146, s[10:11] nt
	s_add_u32 s10, s10, s12
	s_addc_u32 s11, s11, 0
	global_load_dwordx4 v[90:93], v146, s[10:11] nt
	s_add_u32 s10, s10, s12
	s_addc_u32 s11, s11, 0
	global_load_dwordx4 v[94:97], v146, s[10:11] nt
	s_add_u32 s10, s10, s12
	s_addc_u32 s11, s11, 0
	global_load_dwordx4 v[98:101], v146, s[10:11] nt
	s_add_u32 s10, s10, s12
	s_addc_u32 s11, s11, 0
	global_load_dwordx4 v[102:105], v146, s[10:11] nt
	s_add_u32 s10, s10, s12
	s_addc_u32 s11, s11, 0
	global_load_dwordx4 v[106:109], v146, s[10:11] nt
	s_add_u32 s10, s10, s12
	s_addc_u32 s11, s11, 0
	global_load_dwordx4 v[110:113], v146, s[10:11] nt
	s_add_u32 s10, s10, s12
	s_addc_u32 s11, s11, 0
	global_load_dwordx4 v[114:117], v146, s[10:11] nt
	s_add_u32 s10, s10, s12
	s_addc_u32 s11, s11, 0
	global_load_dwordx4 v[118:121], v146, s[10:11] nt
	s_add_u32 s10, s10, s12
	s_addc_u32 s11, s11, 0
	global_load_dwordx4 v[122:125], v146, s[10:11] nt
	s_add_u32 s10, s10, s12
	s_addc_u32 s11, s11, 0
	global_load_dwordx4 v[126:129], v146, s[10:11] nt
	s_add_i32 s32, s32, 64
	s_add_i32 s33, s33, -1
	s_mov_b32 s38, 1
	s_waitcnt vmcnt(16)
.Lcv3_loop:
	s_cmp_lg_u32 s38, 0
	s_cbranch_scc0 .Lcv3_w0A
	s_waitcnt vmcnt(20)
	s_branch .Lcv3_w1A

; #define LAS __attribute__((address_space(3)))
; __device__ __forceinline__ void conv8b_run(const Ctx& X, int first, int step, int count) {
;     ...
;         LAS uchar* buf = X.lds + (j & 1) * CVT_BUF;
; #pragma unroll
;         for (int q = 0; q < 4; ++q) { u32x4 o;
;             o.x = pk_fp8x4(v[0][q] * W8_SCALE, v[1][q] * W8_SCALE, v[2][q] * W8_SCALE, v[3][q] * W8_SCALE); o.y = pk_fp8x4(v[4][q] * W8_SCALE, v[5][q] * W8_SCALE, v[6][q] * W8_SCALE, v[7][q] * W8_SCALE);
;             o.z = pk_fp8x4(v[8][q] * W8_SCALE, v[9][q] * W8_SCALE, v[10][q] * W8_SCALE, v[11][q] * W8_SCALE); o.w = pk_fp8x4(v[12][q] * W8_SCALE, v[13][q] * W8_SCALE, v[14][q] * W8_SCALE, v[15][q] * W8_SCALE);
;             *(LAS u32x4*)(buf + (4 * X.lane + q) * CVT_STRIDE + 16 * X.wave) = o; }
;         if (j + 1 < count) { cn = conv8b_dec(X, first + (j + 1) * step);
; #pragma unroll
;             for (int i = 0; i < 16; ++i) v[i] = __builtin_nontemporal_load((const f32x4*)(cn.W + (size_t)i * cn.N)); }
;         asm volatile("s_waitcnt lgkmcnt(0)" ::: "memory"); __builtin_amdgcn_s_barrier();
; #pragma unroll
;         for (int it = 0; it < 4; ++it) { const u32x4 r = *(const LAS u32x4*)(buf + (32 * X.wave + 8 * it + (X.lane >> 3)) * CVT_STRIDE + 16 * (X.lane & 7));
;             __builtin_nontemporal_store(r, (u32x4*)(c.WT + (size_t)it * 8 * 128)); }
.Lcv3_w1A:
	v_mul_f32_e32 v2, 0x42800000, v2
	v_mul_f32_e32 v6, 0x42800000, v6
	v_med3_f32 v2, v2, s37, v150
	v_med3_f32 v6, v6, s37, v150
	v_mul_f32_e32 v10, 0x42800000, v10
	v_mul_f32_e32 v14, 0x42800000, v14
	v_cvt_pk_fp8_f32 v130, v2, v6
	v_med3_f32 v10, v10, s37, v150
	v_med3_f32 v14, v14, s37, v150
	v_cvt_pk_fp8_f32 v130, v10, v14 op_sel:[0,0,1]
	v_mul_f32_e32 v18, 0x42800000, v18
	v_mul_f32_e32 v22, 0x42800000, v22
	v_med3_f32 v18, v18, s37, v150
	v_med3_f32 v22, v22, s37, v150
	v_mul_f32_e32 v26, 0x42800000, v26
	v_mul_f32_e32 v30, 0x42800000, v30
	v_cvt_pk_fp8_f32 v131, v18, v22
	v_med3_f32 v26, v26, s37, v150
	v_med3_f32 v30, v30, s37, v150
	v_cvt_pk_fp8_f32 v131, v26, v30 op_sel:[0,0,1]
	v_mul_f32_e32 v34, 0x42800000, v34
	v_mul_f32_e32 v38, 0x42800000, v38
	v_med3_f32 v34, v34, s37, v150
	v_med3_f32 v38, v38, s37, v150
	v_mul_f32_e32 v42, 0x42800000, v42
	v_mul_f32_e32 v46, 0x42800000, v46
	v_cvt_pk_fp8_f32 v132, v34, v38
	v_med3_f32 v42, v42, s37, v150
	v_med3_f32 v46, v46, s37, v150
	v_cvt_pk_fp8_f32 v132, v42, v46 op_sel:[0,0,1]
	v_mul_f32_e32 v50, 0x42800000, v50
	v_mul_f32_e32 v54, 0x42800000, v54
	v_med3_f32 v50, v50, s37, v150
	v_med3_f32 v54, v54, s37, v150
	v_mul_f32_e32 v58, 0x42800000, v58
	v_mul_f32_e32 v62, 0x42800000, v62
	v_cvt_pk_fp8_f32 v133, v50, v54
	v_med3_f32 v58, v58, s37, v150
	v_med3_f32 v62, v62, s37, v150
	v_cvt_pk_fp8_f32 v133, v58, v62 op_sel:[0,0,1]
	s_nop 0
	ds_write_b128 v147, v[130:133] offset:0
	v_mul_f32_e32 v3, 0x42800000, v3
	v_mul_f32_e32 v7, 0x42800000, v7
	v_med3_f32 v3, v3, s37, v150
	v_med3_f32 v7, v7, s37, v150
	v_mul_f32_e32 v11, 0x42800000, v11
	v_mul_f32_e32 v15, 0x42800000, v15
	v_cvt_pk_fp8_f32 v134, v3, v7
	v_med3_f32 v11, v11, s37, v150
	v_med3_f32 v15, v15, s37, v150
	v_cvt_pk_fp8_f32 v134, v11, v15 op_sel:[0,0,1]
	v_mul_f32_e32 v19, 0x42800000, v19
	v_mul_f32_e32 v23, 0x42800000, v23
	v_med3_f32 v19, v19, s37, v150
	v_med3_f32 v23, v23, s37, v150
	v_mul_f32_e32 v27, 0x42800000, v27
	v_mul_f32_e32 v31, 0x42800000, v31
	v_cvt_pk_fp8_f32 v135, v19, v23
	v_med3_f32 v27, v27, s37, v150
	v_med3_f32 v31, v31, s37, v150
	v_cvt_pk_fp8_f32 v135, v27, v31 op_sel:[0,0,1]
	v_mul_f32_e32 v35, 0x42800000, v35
	v_mul_f32_e32 v39, 0x42800000, v39
	v_med3_f32 v35, v35, s37, v150
	v_med3_f32 v39, v39, s37, v150
	v_mul_f32_e32 v43, 0x42800000, v43
	v_mul_f32_e32 v47, 0x42800000, v47
	v_cvt_pk_fp8_f32 v136, v35, v39
	v_med3_f32 v43, v43, s37, v150
	v_med3_f32 v47, v47, s37, v150
	v_cvt_pk_fp8_f32 v136, v43, v47 op_sel:[0,0,1]
	v_mul_f32_e32 v51, 0x42800000, v51
	v_mul_f32_e32 v55, 0x42800000, v55
	v_med3_f32 v51, v51, s37, v150
	v_med3_f32 v55, v55, s37, v150
	v_mul_f32_e32 v59, 0x42800000, v59
	v_mul_f32_e32 v63, 0x42800000, v63
	v_cvt_pk_fp8_f32 v137, v51, v55
	v_med3_f32 v59, v59, s37, v150
	v_med3_f32 v63, v63, s37, v150
	v_cvt_pk_fp8_f32 v137, v59, v63 op_sel:[0,0,1]
	s_nop 0
	ds_write_b128 v147, v[134:137] offset:144
	v_mul_f32_e32 v4, 0x42800000, v4
	v_mul_f32_e32 v8, 0x42800000, v8
	v_med3_f32 v4, v4, s37, v150
	v_med3_f32 v8, v8, s37, v150
	v_mul_f32_e32 v12, 0x42800000, v12
	v_mul_f32_e32 v16, 0x42800000, v16
	v_cvt_pk_fp8_f32 v138, v4, v8
	v_med3_f32 v12, v12, s37, v150
	v_med3_f32 v16, v16, s37, v150
	v_cvt_pk_fp8_f32 v138, v12, v16 op_sel:[0,0,1]
	v_mul_f32_e32 v20, 0x42800000, v20
	v_mul_f32_e32 v24, 0x42800000, v24
	v_med3_f32 v20, v20, s37, v150
	v_med3_f32 v24, v24, s37, v150
	v_mul_f32_e32 v28, 0x42800000, v28
	v_mul_f32_e32 v32, 0x42800000, v32
	v_cvt_pk_fp8_f32 v139, v20, v24
	v_med3_f32 v28, v28, s37, v150
	v_med3_f32 v32, v32, s37, v150
	v_cvt_pk_fp8_f32 v139, v28, v32 op_sel:[0,0,1]
	v_mul_f32_e32 v36, 0x42800000, v36
	v_mul_f32_e32 v40, 0x42800000, v40
	v_med3_f32 v36, v36, s37, v150
	v_med3_f32 v40, v40, s37, v150
	v_mul_f32_e32 v44, 0x42800000, v44
	v_mul_f32_e32 v48, 0x42800000, v48
	v_cvt_pk_fp8_f32 v140, v36, v40
	v_med3_f32 v44, v44, s37, v150
	v_med3_f32 v48, v48, s37, v150
	v_cvt_pk_fp8_f32 v140, v44, v48 op_sel:[0,0,1]
	v_mul_f32_e32 v52, 0x42800000, v52
	v_mul_f32_e32 v56, 0x42800000, v56
	v_med3_f32 v52, v52, s37, v150
	v_med3_f32 v56, v56, s37, v150
	v_mul_f32_e32 v60, 0x42800000, v60
	v_mul_f32_e32 v64, 0x42800000, v64
	v_cvt_pk_fp8_f32 v141, v52, v56
	v_med3_f32 v60, v60, s37, v150
	v_med3_f32 v64, v64, s37, v150
	v_cvt_pk_fp8_f32 v141, v60, v64 op_sel:[0,0,1]
	s_nop 0
	ds_write_b128 v147, v[138:141] offset:288
	v_mul_f32_e32 v5, 0x42800000, v5
	v_mul_f32_e32 v9, 0x42800000, v9
	v_med3_f32 v5, v5, s37, v150
	v_med3_f32 v9, v9, s37, v150
	v_mul_f32_e32 v13, 0x42800000, v13
	v_mul_f32_e32 v17, 0x42800000, v17
	v_cvt_pk_fp8_f32 v142, v5, v9
	v_med3_f32 v13, v13, s37, v150
	v_med3_f32 v17, v17, s37, v150
	v_cvt_pk_fp8_f32 v142, v13, v17 op_sel:[0,0,1]
	v_mul_f32_e32 v21, 0x42800000, v21
	v_mul_f32_e32 v25, 0x42800000, v25
	v_med3_f32 v21, v21, s37, v150
	v_med3_f32 v25, v25, s37, v150
	v_mul_f32_e32 v29, 0x42800000, v29
	v_mul_f32_e32 v33, 0x42800000, v33
	v_cvt_pk_fp8_f32 v143, v21, v25
	v_med3_f32 v29, v29, s37, v150
	v_med3_f32 v33, v33, s37, v150
	v_cvt_pk_fp8_f32 v143, v29, v33 op_sel:[0,0,1]
	v_mul_f32_e32 v37, 0x42800000, v37
	v_mul_f32_e32 v41, 0x42800000, v41
	v_med3_f32 v37, v37, s37, v150
	v_med3_f32 v41, v41, s37, v150
	v_mul_f32_e32 v45, 0x42800000, v45
	v_mul_f32_e32 v49, 0x42800000, v49
	v_cvt_pk_fp8_f32 v144, v37, v41
	v_med3_f32 v45, v45, s37, v150
	v_med3_f32 v49, v49, s37, v150
	v_cvt_pk_fp8_f32 v144, v45, v49 op_sel:[0,0,1]
	v_mul_f32_e32 v53, 0x42800000, v53
	v_mul_f32_e32 v57, 0x42800000, v57
	v_med3_f32 v53, v53, s37, v150
	v_med3_f32 v57, v57, s37, v150
	v_mul_f32_e32 v61, 0x42800000, v61
	v_mul_f32_e32 v65, 0x42800000, v65
	v_cvt_pk_fp8_f32 v145, v53, v57
	v_med3_f32 v61, v61, s37, v150
	v_med3_f32 v65, v65, s37, v150
	v_cvt_pk_fp8_f32 v145, v61, v65 op_sel:[0,0,1]
	s_nop 0
	ds_write_b128 v147, v[142:145] offset:432
	s_waitcnt lgkmcnt(0)
	s_barrier
	ds_read_b128 v[130:133], v148 offset:0
	ds_read_b128 v[134:137], v148 offset:1152
	ds_read_b128 v[138:141], v148 offset:2304
	ds_read_b128 v[142:145], v148 offset:3456
	s_waitcnt lgkmcnt(3)
	global_store_dwordx4 v149, v[130:133], s[14:15] nt
	s_waitcnt lgkmcnt(2)
	global_store_dwordx4 v149, v[134:137], s[14:15] offset:1024 nt
	s_waitcnt lgkmcnt(1)
	global_store_dwordx4 v149, v[138:141], s[14:15] offset:2048 nt
	s_waitcnt lgkmcnt(0)
	global_store_dwordx4 v149, v[142:145], s[14:15] offset:3072 nt
	s_cmp_eq_u32 s38, 0
	s_cbranch_scc1 .Lcv3_done
	s_cmp_eq_u32 s33, 0
	s_cbranch_scc1 .Lcv3_nlA
	s_cmp_lt_u32 s32, 0x2000
	s_cbranch_scc0 .Lcv3_dnLA
	s_lshr_b32 s34, s32, 4
	s_lshl_b32 s34, s34, 21
	s_and_b32 s35, s32, 15
	s_lshl_b32 s35, s35, 10
	s_add_u32 s34, s34, s35
	s_lshl_b32 s35, s93, 18
	s_add_u32 s34, s34, s35
	s_add_u32 s10, s6, s34
	s_addc_u32 s11, s7, 0
	s_movk_i32 s12, 0x4000
	s_lshl_b32 s34, s32, 15
	s_add_u32 s34, s34, 0x30000000
	s_branch .Lcv3_cmLA

; __device__ __forceinline__ void conv8b_run(const Ctx& X, int first, int step, int count) {
;     ...
;         if (j + 1 < count) { cn = conv8b_dec(X, first + (j + 1) * step);
; #pragma unroll
;             for (int i = 0; i < 16; ++i) v[i] = __builtin_nontemporal_load((const f32x4*)(cn.W + (size_t)i * cn.N)); }
.Lcv3_cmLA:
	s_lshl_b32 s35, s93, 12
	s_add_u32 s34, s34, s35
	s_add_u32 s14, s90, s34
	s_addc_u32 s15, s91, 0
	global_load_dwordx4 v[2:5], v146, s[10:11] nt
	s_add_u32 s10, s10, s12
	s_addc_u32 s11, s11, 0
	global_load_dwordx4 v[6:9], v146, s[10:11] nt
	s_add_u32 s10, s10, s12
	s_addc_u32 s11, s11, 0
	global_load_dwordx4 v[10:13], v146, s[10:11] nt
	s_add_u32 s10, s10, s12
	s_addc_u32 s11, s11, 0
	global_load_dwordx4 v[14:17], v146, s[10:11] nt
	s_add_u32 s10, s10, s12
	s_addc_u32 s11, s11, 0
	global_load_dwordx4 v[18:21], v146, s[10:11] nt
	s_add_u32 s10, s10, s12
	s_addc_u32 s11, s11, 0
	global_load_dwordx4 v[22:25], v146, s[10:11] nt
	s_add_u32 s10, s10, s12
	s_addc_u32 s11, s11, 0
	global_load_dwordx4 v[26:29], v146, s[10:11] nt
	s_add_u32 s10, s10, s12
	s_addc_u32 s11, s11, 0
	global_load_dwordx4 v[30:33], v146, s[10:11] nt
	s_add_u32 s10, s10, s12
	s_addc_u32 s11, s11, 0
	global_load_dwordx4 v[34:37], v146, s[10:11] nt
	s_add_u32 s10, s10, s12
	s_addc_u32 s11, s11, 0
	global_load_dwordx4 v[38:41], v146, s[10:11] nt
	s_add_u32 s10, s10, s12
	s_addc_u32 s11, s11, 0
	global_load_dwordx4 v[42:45], v146, s[10:11] nt
	s_add_u32 s10, s10, s12
	s_addc_u32 s11, s11, 0
	global_load_dwordx4 v[46:49], v146, s[10:11] nt
	s_add_u32 s10, s10, s12
	s_addc_u32 s11, s11, 0
	global_load_dwordx4 v[50:53], v146, s[10:11] nt
	s_add_u32 s10, s10, s12
	s_addc_u32 s11, s11, 0
	global_load_dwordx4 v[54:57], v146, s[10:11] nt
	s_add_u32 s10, s10, s12
	s_addc_u32 s11, s11, 0
	global_load_dwordx4 v[58:61], v146, s[10:11] nt
	s_add_u32 s10, s10, s12
	s_addc_u32 s11, s11, 0
	global_load_dwordx4 v[62:65], v146, s[10:11] nt
	s_add_i32 s32, s32, 64
	s_add_i32 s33, s33, -1
	s_branch .Lcv3_nxA
.Lcv3_nlA:
	s_mov_b32 s38, 0

; #define LAS __attribute__((address_space(3)))
; __device__ __forceinline__ void conv8b_run(const Ctx& X, int first, int step, int count) {
;     ...
;         LAS uchar* buf = X.lds + (j & 1) * CVT_BUF;
; #pragma unroll
;         for (int q = 0; q < 4; ++q) { u32x4 o;
;             o.x = pk_fp8x4(v[0][q] * W8_SCALE, v[1][q] * W8_SCALE, v[2][q] * W8_SCALE, v[3][q] * W8_SCALE); o.y = pk_fp8x4(v[4][q] * W8_SCALE, v[5][q] * W8_SCALE, v[6][q] * W8_SCALE, v[7][q] * W8_SCALE);
;             o.z = pk_fp8x4(v[8][q] * W8_SCALE, v[9][q] * W8_SCALE, v[10][q] * W8_SCALE, v[11][q] * W8_SCALE); o.w = pk_fp8x4(v[12][q] * W8_SCALE, v[13][q] * W8_SCALE, v[14][q] * W8_SCALE, v[15][q] * W8_SCALE);
;             *(LAS u32x4*)(buf + (4 * X.lane + q) * CVT_STRIDE + 16 * X.wave) = o; }
;         if (j + 1 < count) { cn = conv8b_dec(X, first + (j + 1) * step);
; #pragma unroll
;             for (int i = 0; i < 16; ++i) v[i] = __builtin_nontemporal_load((const f32x4*)(cn.W + (size_t)i * cn.N)); }
;         asm volatile("s_waitcnt lgkmcnt(0)" ::: "memory"); __builtin_amdgcn_s_barrier();
; #pragma unroll
;         for (int it = 0; it < 4; ++it) { const u32x4 r = *(const LAS u32x4*)(buf + (32 * X.wave + 8 * it + (X.lane >> 3)) * CVT_STRIDE + 16 * (X.lane & 7));
;             __builtin_nontemporal_store(r, (u32x4*)(c.WT + (size_t)it * 8 * 128)); }
;         c = cn;
.Lcv3_w1B:
	v_mul_f32_e32 v66, 0x42800000, v66
	v_mul_f32_e32 v70, 0x42800000, v70
	v_med3_f32 v66, v66, s37, v150
	v_med3_f32 v70, v70, s37, v150
	v_mul_f32_e32 v74, 0x42800000, v74
	v_mul_f32_e32 v78, 0x42800000, v78
	v_cvt_pk_fp8_f32 v130, v66, v70
	v_med3_f32 v74, v74, s37, v150
	v_med3_f32 v78, v78, s37, v150
	v_cvt_pk_fp8_f32 v130, v74, v78 op_sel:[0,0,1]
	v_mul_f32_e32 v82, 0x42800000, v82
	v_mul_f32_e32 v86, 0x42800000, v86
	v_med3_f32 v82, v82, s37, v150
	v_med3_f32 v86, v86, s37, v150
	v_mul_f32_e32 v90, 0x42800000, v90
	v_mul_f32_e32 v94, 0x42800000, v94
	v_cvt_pk_fp8_f32 v131, v82, v86
	v_med3_f32 v90, v90, s37, v150
	v_med3_f32 v94, v94, s37, v150
	v_cvt_pk_fp8_f32 v131, v90, v94 op_sel:[0,0,1]
	v_mul_f32_e32 v98, 0x42800000, v98
	v_mul_f32_e32 v102, 0x42800000, v102
	v_med3_f32 v98, v98, s37, v150
	v_med3_f32 v102, v102, s37, v150
	v_mul_f32_e32 v106, 0x42800000, v106
	v_mul_f32_e32 v110, 0x42800000, v110
	v_cvt_pk_fp8_f32 v132, v98, v102
	v_med3_f32 v106, v106, s37, v150
	v_med3_f32 v110, v110, s37, v150
	v_cvt_pk_fp8_f32 v132, v106, v110 op_sel:[0,0,1]
	v_mul_f32_e32 v114, 0x42800000, v114
	v_mul_f32_e32 v118, 0x42800000, v118
	v_med3_f32 v114, v114, s37, v150
	v_med3_f32 v118, v118, s37, v150
	v_mul_f32_e32 v122, 0x42800000, v122
	v_mul_f32_e32 v126, 0x42800000, v126
	v_cvt_pk_fp8_f32 v133, v114, v118
	v_med3_f32 v122, v122, s37, v150
	v_med3_f32 v126, v126, s37, v150
	v_cvt_pk_fp8_f32 v133, v122, v126 op_sel:[0,0,1]
	s_nop 0
	ds_write_b128 v147, v[130:133] offset:36864
	v_mul_f32_e32 v67, 0x42800000, v67
	v_mul_f32_e32 v71, 0x42800000, v71
	v_med3_f32 v67, v67, s37, v150
	v_med3_f32 v71, v71, s37, v150
	v_mul_f32_e32 v75, 0x42800000, v75
	v_mul_f32_e32 v79, 0x42800000, v79
	v_cvt_pk_fp8_f32 v134, v67, v71
	v_med3_f32 v75, v75, s37, v150
	v_med3_f32 v79, v79, s37, v150
	v_cvt_pk_fp8_f32 v134, v75, v79 op_sel:[0,0,1]
	v_mul_f32_e32 v83, 0x42800000, v83
	v_mul_f32_e32 v87, 0x42800000, v87
	v_med3_f32 v83, v83, s37, v150
	v_med3_f32 v87, v87, s37, v150
	v_mul_f32_e32 v91, 0x42800000, v91
	v_mul_f32_e32 v95, 0x42800000, v95
	v_cvt_pk_fp8_f32 v135, v83, v87
	v_med3_f32 v91, v91, s37, v150
	v_med3_f32 v95, v95, s37, v150
	v_cvt_pk_fp8_f32 v135, v91, v95 op_sel:[0,0,1]
	v_mul_f32_e32 v99, 0x42800000, v99
	v_mul_f32_e32 v103, 0x42800000, v103
	v_med3_f32 v99, v99, s37, v150
	v_med3_f32 v103, v103, s37, v150
	v_mul_f32_e32 v107, 0x42800000, v107
	v_mul_f32_e32 v111, 0x42800000, v111
	v_cvt_pk_fp8_f32 v136, v99, v103
	v_med3_f32 v107, v107, s37, v150
	v_med3_f32 v111, v111, s37, v150
	v_cvt_pk_fp8_f32 v136, v107, v111 op_sel:[0,0,1]
	v_mul_f32_e32 v115, 0x42800000, v115
	v_mul_f32_e32 v119, 0x42800000, v119
	v_med3_f32 v115, v115, s37, v150
	v_med3_f32 v119, v119, s37, v150
	v_mul_f32_e32 v123, 0x42800000, v123
	v_mul_f32_e32 v127, 0x42800000, v127
	v_cvt_pk_fp8_f32 v137, v115, v119
	v_med3_f32 v123, v123, s37, v150
	v_med3_f32 v127, v127, s37, v150
	v_cvt_pk_fp8_f32 v137, v123, v127 op_sel:[0,0,1]
	s_nop 0
	ds_write_b128 v147, v[134:137] offset:37008
	v_mul_f32_e32 v68, 0x42800000, v68
	v_mul_f32_e32 v72, 0x42800000, v72
	v_med3_f32 v68, v68, s37, v150
	v_med3_f32 v72, v72, s37, v150
	v_mul_f32_e32 v76, 0x42800000, v76
	v_mul_f32_e32 v80, 0x42800000, v80
	v_cvt_pk_fp8_f32 v138, v68, v72
	v_med3_f32 v76, v76, s37, v150
	v_med3_f32 v80, v80, s37, v150
	v_cvt_pk_fp8_f32 v138, v76, v80 op_sel:[0,0,1]
	v_mul_f32_e32 v84, 0x42800000, v84
	v_mul_f32_e32 v88, 0x42800000, v88
	v_med3_f32 v84, v84, s37, v150
	v_med3_f32 v88, v88, s37, v150
	v_mul_f32_e32 v92, 0x42800000, v92
	v_mul_f32_e32 v96, 0x42800000, v96
	v_cvt_pk_fp8_f32 v139, v84, v88
	v_med3_f32 v92, v92, s37, v150
	v_med3_f32 v96, v96, s37, v150
	v_cvt_pk_fp8_f32 v139, v92, v96 op_sel:[0,0,1]
	v_mul_f32_e32 v100, 0x42800000, v100
	v_mul_f32_e32 v104, 0x42800000, v104
	v_med3_f32 v100, v100, s37, v150
	v_med3_f32 v104, v104, s37, v150
	v_mul_f32_e32 v108, 0x42800000, v108
	v_mul_f32_e32 v112, 0x42800000, v112
	v_cvt_pk_fp8_f32 v140, v100, v104
	v_med3_f32 v108, v108, s37, v150
	v_med3_f32 v112, v112, s37, v150
	v_cvt_pk_fp8_f32 v140, v108, v112 op_sel:[0,0,1]
	v_mul_f32_e32 v116, 0x42800000, v116
	v_mul_f32_e32 v120, 0x42800000, v120
	v_med3_f32 v116, v116, s37, v150
	v_med3_f32 v120, v120, s37, v150
	v_mul_f32_e32 v124, 0x42800000, v124
	v_mul_f32_e32 v128, 0x42800000, v128
	v_cvt_pk_fp8_f32 v141, v116, v120
	v_med3_f32 v124, v124, s37, v150
	v_med3_f32 v128, v128, s37, v150
	v_cvt_pk_fp8_f32 v141, v124, v128 op_sel:[0,0,1]
	s_nop 0
	ds_write_b128 v147, v[138:141] offset:37152
	v_mul_f32_e32 v69, 0x42800000, v69
	v_mul_f32_e32 v73, 0x42800000, v73
	v_med3_f32 v69, v69, s37, v150
	v_med3_f32 v73, v73, s37, v150
	v_mul_f32_e32 v77, 0x42800000, v77
	v_mul_f32_e32 v81, 0x42800000, v81
	v_cvt_pk_fp8_f32 v142, v69, v73
	v_med3_f32 v77, v77, s37, v150
	v_med3_f32 v81, v81, s37, v150
	v_cvt_pk_fp8_f32 v142, v77, v81 op_sel:[0,0,1]
	v_mul_f32_e32 v85, 0x42800000, v85
	v_mul_f32_e32 v89, 0x42800000, v89
	v_med3_f32 v85, v85, s37, v150
	v_med3_f32 v89, v89, s37, v150
	v_mul_f32_e32 v93, 0x42800000, v93
	v_mul_f32_e32 v97, 0x42800000, v97
	v_cvt_pk_fp8_f32 v143, v85, v89
	v_med3_f32 v93, v93, s37, v150
	v_med3_f32 v97, v97, s37, v150
	v_cvt_pk_fp8_f32 v143, v93, v97 op_sel:[0,0,1]
	v_mul_f32_e32 v101, 0x42800000, v101
	v_mul_f32_e32 v105, 0x42800000, v105
	v_med3_f32 v101, v101, s37, v150
	v_med3_f32 v105, v105, s37, v150
	v_mul_f32_e32 v109, 0x42800000, v109
	v_mul_f32_e32 v113, 0x42800000, v113
	v_cvt_pk_fp8_f32 v144, v101, v105
	v_med3_f32 v109, v109, s37, v150
	v_med3_f32 v113, v113, s37, v150
	v_cvt_pk_fp8_f32 v144, v109, v113 op_sel:[0,0,1]
	v_mul_f32_e32 v117, 0x42800000, v117
	v_mul_f32_e32 v121, 0x42800000, v121
	v_med3_f32 v117, v117, s37, v150
	v_med3_f32 v121, v121, s37, v150
	v_mul_f32_e32 v125, 0x42800000, v125
	v_mul_f32_e32 v129, 0x42800000, v129
	v_cvt_pk_fp8_f32 v145, v117, v121
	v_med3_f32 v125, v125, s37, v150
	v_med3_f32 v129, v129, s37, v150
	v_cvt_pk_fp8_f32 v145, v125, v129 op_sel:[0,0,1]
	s_nop 0
	ds_write_b128 v147, v[142:145] offset:37296
	s_waitcnt lgkmcnt(0)
	s_barrier
	ds_read_b128 v[130:133], v148 offset:36864
	ds_read_b128 v[134:137], v148 offset:38016
	ds_read_b128 v[138:141], v148 offset:39168
	ds_read_b128 v[142:145], v148 offset:40320
	s_waitcnt lgkmcnt(3)
	global_store_dwordx4 v149, v[130:133], s[16:17] nt
	s_waitcnt lgkmcnt(2)
	global_store_dwordx4 v149, v[134:137], s[16:17] offset:1024 nt
	s_waitcnt lgkmcnt(1)
	global_store_dwordx4 v149, v[138:141], s[16:17] offset:2048 nt
	s_waitcnt lgkmcnt(0)
	global_store_dwordx4 v149, v[142:145], s[16:17] offset:3072 nt
	s_cmp_eq_u32 s38, 0
	s_cbranch_scc1 .Lcv3_done
	s_cmp_eq_u32 s33, 0
	s_cbranch_scc1 .Lcv3_nlB
	s_cmp_lt_u32 s32, 0x2000
	s_cbranch_scc0 .Lcv3_dnLB
	s_lshr_b32 s34, s32, 4
	s_lshl_b32 s34, s34, 21
	s_and_b32 s35, s32, 15
	s_lshl_b32 s35, s35, 10
	s_add_u32 s34, s34, s35
	s_lshl_b32 s35, s93, 18
	s_add_u32 s34, s34, s35
	s_add_u32 s10, s6, s34
	s_addc_u32 s11, s7, 0
	s_movk_i32 s12, 0x4000
	s_lshl_b32 s34, s32, 15
	s_add_u32 s34, s34, 0x30000000
	s_branch .Lcv3_cmLB

; __device__ __forceinline__ void conv8b_run(const Ctx& X, int first, int step, int count) {
;     ...
;         if (j + 1 < count) { cn = conv8b_dec(X, first + (j + 1) * step);
; #pragma unroll
;             for (int i = 0; i < 16; ++i) v[i] = __builtin_nontemporal_load((const f32x4*)(cn.W + (size_t)i * cn.N)); }
.Lcv3_cmLB:
	s_lshl_b32 s35, s93, 12
	s_add_u32 s34, s34, s35
	s_add_u32 s16, s90, s34
	s_addc_u32 s17, s91, 0
	global_load_dwordx4 v[66:69], v146, s[10:11] nt
	s_add_u32 s10, s10, s12
	s_addc_u32 s11, s11, 0
	global_load_dwordx4 v[70:73], v146, s[10:11] nt
	s_add_u32 s10, s10, s12
	s_addc_u32 s11, s11, 0
	global_load_dwordx4 v[74:77], v146, s[10:11] nt
	s_add_u32 s10, s10, s12
	s_addc_u32 s11, s11, 0
	global_load_dwordx4 v[78:81], v146, s[10:11] nt
	s_add_u32 s10, s10, s12
	s_addc_u32 s11, s11, 0
	global_load_dwordx4 v[82:85], v146, s[10:11] nt
	s_add_u32 s10, s10, s12
	s_addc_u32 s11, s11, 0
	global_load_dwordx4 v[86:89], v146, s[10:11] nt
	s_add_u32 s10, s10, s12
	s_addc_u32 s11, s11, 0
	global_load_dwordx4 v[90:93], v146, s[10:11] nt
	s_add_u32 s10, s10, s12
	s_addc_u32 s11, s11, 0
	global_load_dwordx4 v[94:97], v146, s[10:11] nt
	s_add_u32 s10, s10, s12
	s_addc_u32 s11, s11, 0
	global_load_dwordx4 v[98:101], v146, s[10:11] nt
	s_add_u32 s10, s10, s12
	s_addc_u32 s11, s11, 0
	global_load_dwordx4 v[102:105], v146, s[10:11] nt
	s_add_u32 s10, s10, s12
	s_addc_u32 s11, s11, 0
	global_load_dwordx4 v[106:109], v146, s[10:11] nt
	s_add_u32 s10, s10, s12
	s_addc_u32 s11, s11, 0
	global_load_dwordx4 v[110:113], v146, s[10:11] nt
	s_add_u32 s10, s10, s12
	s_addc_u32 s11, s11, 0
	global_load_dwordx4 v[114:117], v146, s[10:11] nt
	s_add_u32 s10, s10, s12
	s_addc_u32 s11, s11, 0
	global_load_dwordx4 v[118:121], v146, s[10:11] nt
	s_add_u32 s10, s10, s12
	s_addc_u32 s11, s11, 0
	global_load_dwordx4 v[122:125], v146, s[10:11] nt
	s_add_u32 s10, s10, s12
	s_addc_u32 s11, s11, 0
	global_load_dwordx4 v[126:129], v146, s[10:11] nt
	s_add_i32 s32, s32, 64
	s_add_i32 s33, s33, -1
	s_branch .Lcv3_nxB

; __device__ __forceinline__ void conv8b_run(const Ctx& X, int first, int step, int count) {
;     ...
;     asm volatile("s_waitcnt lgkmcnt(0)" ::: "memory"); __builtin_amdgcn_s_barrier();
.Lcv3_done:
.LBB0_479:
	s_waitcnt lgkmcnt(0)
	s_barrier
